# attention phase: one static s_setprio 1 for waves 4-7 before the task loop (reset at phase exit)
# baseline (speedup 1.0000x reference)
.Lfa_entry:
	s_waitcnt lgkmcnt(0)
	s_load_dwordx2 s[0:1], s[30:31], 0xd8
	v_mbcnt_lo_u32_b32 v0, -1, 0
	v_mbcnt_hi_u32_b32 v0, -1, v0
	s_lshr_b32 s15, s3, 6
	s_cmp_ge_u32 s15, 4
	s_cbranch_scc0 .Lfa_prio_done
	s_setprio 1
.Lfa_prio_done:
	s_lshl_b32 s20, s15, 10
	s_mul_i32 s21, s15, 0xc00
	s_add_i32 s21, s21, 0x18800
	v_lshlrev_b32_e32 v1, 2, v0
	v_add_u32_e32 v1, s21, v1
	ds_write_b32 v1, v162 offset:0
	ds_write_b32 v1, v163 offset:256
	ds_write_b32 v1, v164 offset:512
	ds_write_b32 v1, v165 offset:768
	ds_write_b32 v1, v166 offset:1024
	ds_write_b32 v1, v167 offset:1280
	ds_write_b32 v1, v168 offset:1536
	ds_write_b32 v1, v169 offset:1792
	ds_write_b32 v1, v170 offset:2048
	ds_write_b32 v1, v171 offset:2304
	ds_write_b32 v1, v172 offset:2560
	ds_write_b32 v1, v173 offset:2816
	v_and_b32_e32 v2, 31, v0
	v_lshrrev_b32_e32 v3, 5, v0
	v_lshlrev_b32_e32 v208, 8, v2
	v_and_b32_e32 v4, 7, v2
	v_lshlrev_b32_e32 v4, 4, v4
	v_lshlrev_b32_e32 v5, 4, v3
	v_xor_b32_e32 v209, v4, v5
	v_and_b32_e32 v4, 3, v0
	v_lshlrev_b32_e32 v4, 3, v4
	v_bfe_u32 v5, v0, 2, 2
	v_lshl_or_b32 v4, v5, 6, v4
	v_bfe_u32 v5, v0, 4, 1
	v_lshl_or_b32 v4, v5, 5, v4
	v_lshl_or_b32 v210, v3, 8, v4
	s_add_i32 s21, s20, 0x1e800
	v_lshl_add_u32 v11, v0, 2, s21
	v_lshrrev_b32_e32 v4, 4, v0
	v_and_b32_e32 v5, 15, v0
	s_add_i32 s21, s15, 0
	s_lshl_b32 s21, s21, 2
	v_add_u32_e32 v6, s21, v4
	v_and_b32_e32 v7, 7, v6
	v_xor_b32_e32 v7, v5, v7
	v_lshlrev_b32_e32 v7, 4, v7
	v_lshl_or_b32 v12, v6, 8, v7
	ds_write_b32 v11, v12 offset:0
	s_add_i32 s21, s15, 8
	s_lshl_b32 s21, s21, 2
	v_add_u32_e32 v6, s21, v4
	v_and_b32_e32 v7, 7, v6
	v_xor_b32_e32 v7, v5, v7
	v_lshlrev_b32_e32 v7, 4, v7
	v_lshl_or_b32 v12, v6, 8, v7
	ds_write_b32 v11, v12 offset:256
	v_bfe_u32 v4, v0, 2, 3
	v_and_b32_e32 v5, 3, v0
	v_lshlrev_b32_e32 v5, 4, v5
	s_add_i32 s21, s15, 0
	s_lshl_b32 s21, s21, 1
	v_add_u32_e32 v6, s21, v3
	v_lshrrev_b32_e32 v7, 2, v6
	v_lshl_or_b32 v7, v7, 3, v4
	v_and_b32_e32 v8, 3, v6
	v_lshl_or_b32 v8, v8, 6, v5
	v_and_b32_e32 v9, 0xfffffff3, v7
	v_bfe_u32 v10, v7, 2, 1
	v_lshl_or_b32 v9, v10, 3, v9
	v_bfe_u32 v10, v7, 3, 1
	v_lshl_or_b32 v9, v10, 2, v9
	v_lshl_or_b32 v12, v9, 8, v8
	ds_write_b32 v11, v12 offset:512
	s_add_i32 s21, s15, 8
	s_lshl_b32 s21, s21, 1
	v_add_u32_e32 v6, s21, v3
	v_lshrrev_b32_e32 v7, 2, v6
	v_lshl_or_b32 v7, v7, 3, v4
	v_and_b32_e32 v8, 3, v6
	v_lshl_or_b32 v8, v8, 6, v5
	v_and_b32_e32 v9, 0xfffffff3, v7
	v_bfe_u32 v10, v7, 2, 1
	v_lshl_or_b32 v9, v10, 3, v9
	v_bfe_u32 v10, v7, 3, 1
	v_lshl_or_b32 v9, v10, 2, v9
	v_lshl_or_b32 v12, v9, 8, v8
	ds_write_b32 v11, v12 offset:768
	s_waitcnt lgkmcnt(0)
	s_load_dwordx2 s[48:49], s[30:31], 0x90
	s_sub_i32 s21, s11, 2
	s_lshl_b32 s52, s21, 11
	v_lshlrev_b32_e32 v12, 2, v0
	s_waitcnt lgkmcnt(0)
	s_add_u32 s48, s48, s52
	s_addc_u32 s49, s49, 0
	global_load_dword v4, v12, s[48:49] offset:0
	global_load_dword v5, v12, s[48:49] offset:256
	global_load_dword v6, v12, s[48:49] offset:512
	global_load_dword v7, v12, s[48:49] offset:768
	global_load_dword v8, v12, s[48:49] offset:1024
	global_load_dword v9, v12, s[48:49] offset:1280
	global_load_dword v10, v12, s[48:49] offset:1536
	global_load_dword v11, v12, s[48:49] offset:1792
	s_waitcnt vmcnt(0)
	v_mul_f32_e32 v13, v4, v6
	v_fmac_f32_e32 v13, v5, v7
	v_mul_f32_e32 v14, v8, v10
	v_fmac_f32_e32 v14, v9, v11
	s_nop 1
	v_add_f32_dpp v13, v13, v13 quad_perm:[1,0,3,2] row_mask:0xf bank_mask:0xf bound_ctrl:1
	s_nop 1
	v_add_f32_dpp v13, v13, v13 quad_perm:[2,3,0,1] row_mask:0xf bank_mask:0xf bound_ctrl:1
	s_nop 1
	v_add_f32_dpp v13, v13, v13 row_half_mirror row_mask:0xf bank_mask:0xf bound_ctrl:1
	s_nop 1
	v_add_f32_dpp v13, v13, v13 row_mirror row_mask:0xf bank_mask:0xf bound_ctrl:1
	v_mov_b32_e32 v15, 0
	s_nop 1
	v_mov_b32_dpp v15, v13 row_bcast:15 row_mask:0xa bank_mask:0xf
	v_add_f32_e32 v13, v13, v15
	v_mov_b32_e32 v15, 0
	s_nop 1
	v_mov_b32_dpp v15, v13 row_bcast:31 row_mask:0xc bank_mask:0xf
	v_add_f32_e32 v13, v13, v15
	s_nop 1
	v_readlane_b32 s48, v13, 63
	s_nop 1
	v_add_f32_dpp v14, v14, v14 quad_perm:[1,0,3,2] row_mask:0xf bank_mask:0xf bound_ctrl:1
	s_nop 1
	v_add_f32_dpp v14, v14, v14 quad_perm:[2,3,0,1] row_mask:0xf bank_mask:0xf bound_ctrl:1
	s_nop 1
	v_add_f32_dpp v14, v14, v14 row_half_mirror row_mask:0xf bank_mask:0xf bound_ctrl:1
	s_nop 1
	v_add_f32_dpp v14, v14, v14 row_mirror row_mask:0xf bank_mask:0xf bound_ctrl:1
	v_mov_b32_e32 v15, 0
	s_nop 1
	v_mov_b32_dpp v15, v14 row_bcast:15 row_mask:0xa bank_mask:0xf
	v_add_f32_e32 v14, v14, v15
	v_mov_b32_e32 v15, 0
	s_nop 1
	v_mov_b32_dpp v15, v14 row_bcast:31 row_mask:0xc bank_mask:0xf
	v_add_f32_e32 v14, v14, v15
	s_nop 1
	v_readlane_b32 s49, v14, 63
	s_nop 1
	v_mov_b32_e32 v13, s48
	v_mov_b32_e32 v14, s49
	v_mul_f32_e32 v13, 0x3fb8aa3b, v13
	v_mul_f32_e32 v14, 0x3fb8aa3b, v14
	v_exp_f32_e32 v13, v13
	v_exp_f32_e32 v14, v14
	s_mov_b32 s21, 0x3f0e59d5
	s_mov_b32 s52, 0x3ef1014c
	s_cmp_eq_u32 s11, 2
	s_cselect_b32 s21, s52, s21
	v_sub_f32_e32 v13, v13, v14
	v_add_f32_e32 v13, s21, v13
	v_sub_f32_e64 v14, 1.0, s21
	s_nop 0
	v_readfirstlane_b32 s79, v13
	v_readfirstlane_b32 s88, v14
	s_mov_b32 s2, s94

.Lfa_done:
	s_setprio 0
	s_waitcnt vmcnt(0) lgkmcnt(0)
	v_mbcnt_lo_u32_b32 v0, -1, 0
	v_mbcnt_hi_u32_b32 v0, -1, v0
	s_mul_i32 s21, s15, 0xc00
	s_add_i32 s21, s21, 0x18800
	v_lshlrev_b32_e32 v1, 2, v0
	v_add_u32_e32 v1, s21, v1
	ds_read_b32 v162, v1 offset:0
	ds_read_b32 v163, v1 offset:256
	ds_read_b32 v164, v1 offset:512
	ds_read_b32 v165, v1 offset:768
	ds_read_b32 v166, v1 offset:1024
	ds_read_b32 v167, v1 offset:1280
	ds_read_b32 v168, v1 offset:1536
	ds_read_b32 v169, v1 offset:1792
	ds_read_b32 v170, v1 offset:2048
	ds_read_b32 v171, v1 offset:2304
	ds_read_b32 v172, v1 offset:2560
	ds_read_b32 v173, v1 offset:2816
	v_mov_b32_e32 v214, 0x3f4ccccd
	v_mov_b32_e32 v215, 0xff800000
	v_mov_b32_e32 v216, 0xbf3a00e3
	v_mov_b32_e32 v217, 0x3a000000
	v_mov_b32_e32 v218, 0xf149f2ca
	v_mov_b32_e32 v219, 0x7f800000
	v_mov_b32_e32 v220, 0x3fb8aa3b
	v_mov_b32_e32 v221, 0x32a5705f
	v_mov_b32_e32 v222, 0xc2ce8ed0
	v_mov_b32_e32 v223, 0x42b17218
	v_mov_b32_e32 v224, 0x3b800000
	v_mov_b32_e32 v225, 0x41b17218
	v_mov_b32_e32 v226, 0x4200
	v_mov_b32_e32 v227, 0x34000
	s_waitcnt lgkmcnt(0)
